# P2 in-proj epilogue stores PROJB with sc1 (write-through; next read in P3 behind a grid barrier)
# speedup vs baseline: 1.0026x; 1.0008x over previous
.LBB0_339:
	v_mov_b64_e32 v[138:139], s[20:21]
	v_mad_i64_i32 v[138:139], s[6:7], v136, s51, v[138:139]
	v_cndmask_b32_e64 v137, 0, 1, s[8:9]
	v_lshl_add_u64 v[138:139], v[146:147], 1, v[138:139]
	v_cvt_pk_bf16_f32 v140, v153, v165
	v_cvt_pk_bf16_f32 v141, v168, v169
	v_cvt_pk_bf16_f32 v142, v152, v164
	v_cvt_pk_bf16_f32 v143, v166, v167
	s_waitcnt vmcnt(0)
	v_pk_add_f32 v[134:135], v[134:135], v[30:31]
	v_pk_add_f32 v[132:133], v[132:133], v[28:29]
	v_pk_add_f32 v[130:131], v[130:131], v[26:27]
	v_pk_add_f32 v[128:129], v[128:129], v[24:25]
	v_cmp_ne_u32_e64 s[6:7], 1, v137
	s_andn2_b64 vcc, exec, s[8:9]
	s_mov_b64 s[8:9], -1
	global_store_dwordx4 v[138:139], v[140:143], off sc1
	s_cbranch_vccnz .LBB0_343
	s_and_b64 vcc, exec, s[4:5]
	v_mov_b32_e32 v149, v131
	v_mov_b32_e32 v148, v130
	v_mov_b32_e32 v141, v129
	v_mov_b32_e32 v140, v128
	v_mov_b32_e32 v153, v135
	v_mov_b32_e32 v152, v134
	v_mov_b32_e32 v143, v133
	v_mov_b32_e32 v142, v132
	s_cbranch_vccnz .LBB0_342
	v_mul_f32_e32 v137, 0xbfb8aa3b, v132
	v_exp_f32_e32 v137, v137
	v_mul_f32_e32 v141, 0xbfb8aa3b, v129
	v_exp_f32_e32 v141, v141
	v_mul_f32_e32 v140, 0xbfb8aa3b, v128
	v_add_f32_e32 v137, 1.0, v137
	v_rcp_f32_e32 v142, v137
	v_mul_f32_e32 v137, 0xbfb8aa3b, v133
	v_exp_f32_e32 v137, v137
	v_exp_f32_e32 v140, v140
	v_add_f32_e32 v137, 1.0, v137
	v_rcp_f32_e32 v143, v137
	v_add_f32_e32 v137, 1.0, v141
	v_mul_f32_e32 v141, 0xbfb8aa3b, v134
	v_exp_f32_e32 v148, v141
	v_mul_f32_e32 v141, 0xbfb8aa3b, v130
	v_exp_f32_e32 v149, v141
	v_rcp_f32_e32 v141, v137
	v_add_f32_e32 v137, 1.0, v148
	v_mul_f32_e32 v148, 0xbfb8aa3b, v135
	v_rcp_f32_e32 v152, v137
	v_add_f32_e32 v137, 1.0, v149
	v_exp_f32_e32 v149, v148
	v_mul_f32_e32 v148, 0xbfb8aa3b, v131
	v_exp_f32_e32 v164, v148
	v_rcp_f32_e32 v148, v137
	v_add_f32_e32 v137, 1.0, v149
	v_add_f32_e32 v140, 1.0, v140
	v_rcp_f32_e32 v153, v137
	v_add_f32_e32 v137, 1.0, v164
	v_rcp_f32_e32 v140, v140
	v_rcp_f32_e32 v149, v137

.LBB0_347:
	s_nop 0
	v_cvt_pk_bf16_f32 v128, v142, v143
	v_cvt_pk_bf16_f32 v129, v152, v153
	v_cvt_pk_bf16_f32 v130, v140, v141
	v_cvt_pk_bf16_f32 v131, v148, v149
	global_store_dwordx4 v[138:139], v[128:131], off offset:256 sc1
	v_pk_add_f32 v[124:125], v[124:125], v[44:45]
	s_andn2_b64 vcc, exec, s[30:31]
	v_pk_add_f32 v[128:129], v[126:127], v[46:47]
	v_pk_add_f32 v[126:127], v[122:123], v[42:43]
	v_pk_add_f32 v[122:123], v[120:121], v[40:41]
	v_cndmask_b32_e64 v120, 0, 1, s[30:31]
	v_cmp_ne_u32_e64 s[8:9], 1, v120
	s_mov_b64 s[30:31], -1
	s_cbranch_vccnz .LBB0_351
	s_and_b64 vcc, exec, s[4:5]
	v_mov_b32_e32 v138, v127
	v_mov_b32_e32 v137, v126
	v_mov_b32_e32 v134, v123
	v_mov_b32_e32 v132, v122
	v_mov_b32_e32 v140, v129
	v_mov_b32_e32 v139, v128
	v_mov_b32_e32 v135, v125
	v_mov_b32_e32 v133, v124
	s_cbranch_vccnz .LBB0_350
	v_mul_f32_e32 v120, 0xbfb8aa3b, v124
	v_exp_f32_e32 v120, v120
	v_mul_f32_e32 v121, 0xbfb8aa3b, v122
	v_exp_f32_e32 v121, v121
	v_mul_f32_e32 v130, 0xbfb8aa3b, v123
	v_add_f32_e32 v120, 1.0, v120
	v_rcp_f32_e32 v133, v120
	v_mul_f32_e32 v120, 0xbfb8aa3b, v125
	v_exp_f32_e32 v120, v120
	v_exp_f32_e32 v130, v130
	v_add_f32_e32 v121, 1.0, v121
	v_rcp_f32_e32 v132, v121
	v_add_f32_e32 v120, 1.0, v120
	v_mul_f32_e32 v121, 0xbfb8aa3b, v128
	v_rcp_f32_e32 v135, v120
	v_add_f32_e32 v120, 1.0, v130
	v_exp_f32_e32 v121, v121
	v_mul_f32_e32 v130, 0xbfb8aa3b, v126
	v_exp_f32_e32 v130, v130
	v_rcp_f32_e32 v134, v120
	v_add_f32_e32 v120, 1.0, v121
	v_mul_f32_e32 v121, 0xbfb8aa3b, v129
	v_rcp_f32_e32 v139, v120
	v_add_f32_e32 v120, 1.0, v130
	v_exp_f32_e32 v121, v121
	v_mul_f32_e32 v130, 0xbfb8aa3b, v127
	v_exp_f32_e32 v130, v130
	v_rcp_f32_e32 v137, v120
	v_add_f32_e32 v120, 1.0, v121
	v_rcp_f32_e32 v140, v120
	v_add_f32_e32 v120, 1.0, v130
	v_rcp_f32_e32 v138, v120

.LBB0_357:
	v_mov_b64_e32 v[122:123], s[20:21]
	v_mad_i64_i32 v[122:123], s[30:31], v130, s51, v[122:123]
	v_lshl_add_u64 v[122:123], v[146:147], 1, v[122:123]
	v_cvt_pk_bf16_f32 v124, v133, v135
	v_cvt_pk_bf16_f32 v125, v139, v140
	v_cvt_pk_bf16_f32 v126, v132, v134
	v_cvt_pk_bf16_f32 v127, v137, v138
	v_pk_add_f32 v[118:119], v[118:119], v[30:31]
	v_pk_add_f32 v[116:117], v[116:117], v[28:29]
	v_pk_add_f32 v[114:115], v[114:115], v[26:27]
	v_pk_add_f32 v[112:113], v[112:113], v[24:25]
	s_and_b64 vcc, exec, s[6:7]
	s_mov_b64 s[30:31], -1
	global_store_dwordx4 v[122:123], v[124:127], off sc1
	s_cbranch_vccnz .LBB0_361
	s_and_b64 vcc, exec, s[4:5]
	v_mov_b32_e32 v129, v115
	v_mov_b32_e32 v128, v114
	v_mov_b32_e32 v125, v113
	v_mov_b32_e32 v124, v112
	v_mov_b32_e32 v131, v119
	v_mov_b32_e32 v130, v118
	v_mov_b32_e32 v127, v117
	v_mov_b32_e32 v126, v116
	s_cbranch_vccnz .LBB0_360
	v_mul_f32_e32 v124, 0xbfb8aa3b, v116
	v_exp_f32_e32 v124, v124
	v_mul_f32_e32 v125, 0xbfb8aa3b, v112
	v_exp_f32_e32 v125, v125
	v_mul_f32_e32 v129, 0xbfb8aa3b, v114
	v_add_f32_e32 v124, 1.0, v124
	v_rcp_f32_e32 v126, v124
	v_mul_f32_e32 v124, 0xbfb8aa3b, v117
	v_exp_f32_e32 v127, v124
	v_mul_f32_e32 v124, 0xbfb8aa3b, v113
	v_exp_f32_e32 v128, v124
	v_add_f32_e32 v125, 1.0, v125
	v_rcp_f32_e32 v124, v125
	v_add_f32_e32 v125, 1.0, v127
	v_rcp_f32_e32 v127, v125
	v_add_f32_e32 v125, 1.0, v128
	v_mul_f32_e32 v128, 0xbfb8aa3b, v118
	v_exp_f32_e32 v128, v128
	v_exp_f32_e32 v129, v129
	v_mul_f32_e32 v131, 0xbfb8aa3b, v115
	v_exp_f32_e32 v132, v131
	v_add_f32_e32 v128, 1.0, v128
	v_rcp_f32_e32 v130, v128
	v_add_f32_e32 v128, 1.0, v129
	v_mul_f32_e32 v129, 0xbfb8aa3b, v119
	v_exp_f32_e32 v129, v129
	v_rcp_f32_e32 v125, v125
	v_rcp_f32_e32 v128, v128
	v_add_f32_e32 v129, 1.0, v129
	v_rcp_f32_e32 v131, v129
	v_add_f32_e32 v129, 1.0, v132
	v_rcp_f32_e32 v129, v129

.LBB0_365:
	s_nop 0
	v_cvt_pk_bf16_f32 v112, v126, v127
	v_cvt_pk_bf16_f32 v113, v130, v131
	v_cvt_pk_bf16_f32 v114, v124, v125
	v_cvt_pk_bf16_f32 v115, v128, v129
	global_store_dwordx4 v[122:123], v[112:115], off offset:256 sc1
	v_pk_add_f32 v[108:109], v[108:109], v[44:45]
	s_and_b64 vcc, exec, s[8:9]
	v_pk_add_f32 v[112:113], v[110:111], v[46:47]
	v_pk_add_f32 v[110:111], v[106:107], v[42:43]
	v_pk_add_f32 v[106:107], v[104:105], v[40:41]
	s_mov_b64 s[30:31], -1
	s_cbranch_vccnz .LBB0_369
	s_and_b64 vcc, exec, s[4:5]
	v_mov_b32_e32 v121, v111
	v_mov_b32_e32 v120, v110
	v_mov_b32_e32 v118, v107
	v_mov_b32_e32 v116, v106
	v_mov_b32_e32 v123, v113
	v_mov_b32_e32 v122, v112
	v_mov_b32_e32 v119, v109
	v_mov_b32_e32 v117, v108
	s_cbranch_vccnz .LBB0_368
	v_mul_f32_e32 v104, 0xbfb8aa3b, v108
	v_exp_f32_e32 v104, v104
	v_mul_f32_e32 v105, 0xbfb8aa3b, v106
	v_exp_f32_e32 v105, v105
	v_mul_f32_e32 v114, 0xbfb8aa3b, v107
	v_add_f32_e32 v104, 1.0, v104
	v_rcp_f32_e32 v117, v104
	v_mul_f32_e32 v104, 0xbfb8aa3b, v109
	v_exp_f32_e32 v104, v104
	v_exp_f32_e32 v114, v114
	v_add_f32_e32 v105, 1.0, v105
	v_rcp_f32_e32 v116, v105
	v_add_f32_e32 v104, 1.0, v104
	v_mul_f32_e32 v105, 0xbfb8aa3b, v112
	v_rcp_f32_e32 v119, v104
	v_add_f32_e32 v104, 1.0, v114
	v_exp_f32_e32 v105, v105
	v_mul_f32_e32 v114, 0xbfb8aa3b, v110
	v_exp_f32_e32 v114, v114
	v_rcp_f32_e32 v118, v104
	v_add_f32_e32 v104, 1.0, v105
	v_mul_f32_e32 v105, 0xbfb8aa3b, v113
	v_rcp_f32_e32 v122, v104
	v_add_f32_e32 v104, 1.0, v114
	v_exp_f32_e32 v105, v105
	v_mul_f32_e32 v114, 0xbfb8aa3b, v111
	v_exp_f32_e32 v114, v114
	v_rcp_f32_e32 v120, v104
	v_add_f32_e32 v104, 1.0, v105
	v_rcp_f32_e32 v123, v104
	v_add_f32_e32 v104, 1.0, v114
	v_rcp_f32_e32 v121, v104

.LBB0_375:
	v_mov_b64_e32 v[106:107], s[20:21]
	v_mad_i64_i32 v[106:107], s[30:31], v114, s51, v[106:107]
	v_lshl_add_u64 v[106:107], v[146:147], 1, v[106:107]
	v_cvt_pk_bf16_f32 v108, v117, v119
	v_cvt_pk_bf16_f32 v109, v122, v123
	v_cvt_pk_bf16_f32 v110, v116, v118
	v_cvt_pk_bf16_f32 v111, v120, v121
	v_pk_add_f32 v[102:103], v[102:103], v[30:31]
	v_pk_add_f32 v[100:101], v[100:101], v[28:29]
	v_pk_add_f32 v[98:99], v[98:99], v[26:27]
	v_pk_add_f32 v[96:97], v[96:97], v[24:25]
	s_and_b64 vcc, exec, s[6:7]
	s_mov_b64 s[30:31], -1
	global_store_dwordx4 v[106:107], v[108:111], off sc1
	s_cbranch_vccnz .LBB0_379
	s_and_b64 vcc, exec, s[4:5]
	v_mov_b32_e32 v113, v99
	v_mov_b32_e32 v112, v98
	v_mov_b32_e32 v109, v97
	v_mov_b32_e32 v108, v96
	v_mov_b32_e32 v115, v103
	v_mov_b32_e32 v114, v102
	v_mov_b32_e32 v111, v101
	v_mov_b32_e32 v110, v100
	s_cbranch_vccnz .LBB0_378
	v_mul_f32_e32 v108, 0xbfb8aa3b, v100
	v_exp_f32_e32 v108, v108
	v_mul_f32_e32 v109, 0xbfb8aa3b, v96
	v_exp_f32_e32 v109, v109
	v_mul_f32_e32 v113, 0xbfb8aa3b, v98
	v_add_f32_e32 v108, 1.0, v108
	v_rcp_f32_e32 v110, v108
	v_mul_f32_e32 v108, 0xbfb8aa3b, v101
	v_exp_f32_e32 v111, v108
	v_mul_f32_e32 v108, 0xbfb8aa3b, v97
	v_exp_f32_e32 v112, v108
	v_add_f32_e32 v109, 1.0, v109
	v_rcp_f32_e32 v108, v109
	v_add_f32_e32 v109, 1.0, v111
	v_rcp_f32_e32 v111, v109
	v_add_f32_e32 v109, 1.0, v112
	v_mul_f32_e32 v112, 0xbfb8aa3b, v102
	v_exp_f32_e32 v112, v112
	v_exp_f32_e32 v113, v113
	v_mul_f32_e32 v115, 0xbfb8aa3b, v99
	v_exp_f32_e32 v116, v115
	v_add_f32_e32 v112, 1.0, v112
	v_rcp_f32_e32 v114, v112
	v_add_f32_e32 v112, 1.0, v113
	v_mul_f32_e32 v113, 0xbfb8aa3b, v103
	v_exp_f32_e32 v113, v113
	v_rcp_f32_e32 v109, v109
	v_rcp_f32_e32 v112, v112
	v_add_f32_e32 v113, 1.0, v113
	v_rcp_f32_e32 v115, v113
	v_add_f32_e32 v113, 1.0, v116
	v_rcp_f32_e32 v113, v113

.LBB0_383:
	s_nop 0
	v_cvt_pk_bf16_f32 v96, v110, v111
	v_cvt_pk_bf16_f32 v97, v114, v115
	v_cvt_pk_bf16_f32 v98, v108, v109
	v_cvt_pk_bf16_f32 v99, v112, v113
	global_store_dwordx4 v[106:107], v[96:99], off offset:256 sc1
	v_pk_add_f32 v[92:93], v[92:93], v[44:45]
	s_and_b64 vcc, exec, s[8:9]
	v_pk_add_f32 v[96:97], v[94:95], v[46:47]
	v_pk_add_f32 v[94:95], v[90:91], v[42:43]
	v_pk_add_f32 v[90:91], v[88:89], v[40:41]
	s_mov_b64 s[30:31], -1
	s_cbranch_vccnz .LBB0_387
	s_and_b64 vcc, exec, s[4:5]
	v_mov_b32_e32 v105, v95
	v_mov_b32_e32 v104, v94
	v_mov_b32_e32 v102, v91
	v_mov_b32_e32 v100, v90
	v_mov_b32_e32 v107, v97
	v_mov_b32_e32 v106, v96
	v_mov_b32_e32 v103, v93
	v_mov_b32_e32 v101, v92
	s_cbranch_vccnz .LBB0_386
	v_mul_f32_e32 v88, 0xbfb8aa3b, v92
	v_exp_f32_e32 v88, v88
	v_mul_f32_e32 v89, 0xbfb8aa3b, v90
	v_exp_f32_e32 v89, v89
	v_mul_f32_e32 v98, 0xbfb8aa3b, v91
	v_add_f32_e32 v88, 1.0, v88
	v_rcp_f32_e32 v101, v88
	v_mul_f32_e32 v88, 0xbfb8aa3b, v93
	v_exp_f32_e32 v88, v88
	v_exp_f32_e32 v98, v98
	v_add_f32_e32 v89, 1.0, v89
	v_rcp_f32_e32 v100, v89
	v_add_f32_e32 v88, 1.0, v88
	v_mul_f32_e32 v89, 0xbfb8aa3b, v96
	v_rcp_f32_e32 v103, v88
	v_add_f32_e32 v88, 1.0, v98
	v_exp_f32_e32 v89, v89
	v_mul_f32_e32 v98, 0xbfb8aa3b, v94
	v_exp_f32_e32 v98, v98
	v_rcp_f32_e32 v102, v88
	v_add_f32_e32 v88, 1.0, v89
	v_mul_f32_e32 v89, 0xbfb8aa3b, v97
	v_rcp_f32_e32 v106, v88
	v_add_f32_e32 v88, 1.0, v98
	v_exp_f32_e32 v89, v89
	v_mul_f32_e32 v98, 0xbfb8aa3b, v95
	v_exp_f32_e32 v98, v98
	v_rcp_f32_e32 v104, v88
	v_add_f32_e32 v88, 1.0, v89
	v_rcp_f32_e32 v107, v88
	v_add_f32_e32 v88, 1.0, v98
	v_rcp_f32_e32 v105, v88

.LBB0_393:
	v_mov_b64_e32 v[90:91], s[20:21]
	v_mad_i64_i32 v[90:91], s[30:31], v98, s51, v[90:91]
	v_lshl_add_u64 v[90:91], v[146:147], 1, v[90:91]
	v_cvt_pk_bf16_f32 v92, v101, v103
	v_cvt_pk_bf16_f32 v93, v106, v107
	v_cvt_pk_bf16_f32 v94, v100, v102
	v_cvt_pk_bf16_f32 v95, v104, v105
	v_pk_add_f32 v[86:87], v[86:87], v[30:31]
	v_pk_add_f32 v[84:85], v[84:85], v[28:29]
	v_pk_add_f32 v[82:83], v[82:83], v[26:27]
	v_pk_add_f32 v[80:81], v[80:81], v[24:25]
	s_and_b64 vcc, exec, s[6:7]
	s_mov_b64 s[30:31], -1
	global_store_dwordx4 v[90:91], v[92:95], off sc1
	s_cbranch_vccnz .LBB0_397
	s_and_b64 vcc, exec, s[4:5]
	v_mov_b32_e32 v97, v83
	v_mov_b32_e32 v96, v82
	v_mov_b32_e32 v93, v81
	v_mov_b32_e32 v92, v80
	v_mov_b32_e32 v99, v87
	v_mov_b32_e32 v98, v86
	v_mov_b32_e32 v95, v85
	v_mov_b32_e32 v94, v84
	s_cbranch_vccnz .LBB0_396
	v_mul_f32_e32 v92, 0xbfb8aa3b, v84
	v_exp_f32_e32 v92, v92
	v_mul_f32_e32 v93, 0xbfb8aa3b, v80
	v_exp_f32_e32 v93, v93
	v_mul_f32_e32 v97, 0xbfb8aa3b, v82
	v_add_f32_e32 v92, 1.0, v92
	v_rcp_f32_e32 v94, v92
	v_mul_f32_e32 v92, 0xbfb8aa3b, v85
	v_exp_f32_e32 v95, v92
	v_mul_f32_e32 v92, 0xbfb8aa3b, v81
	v_exp_f32_e32 v96, v92
	v_add_f32_e32 v93, 1.0, v93
	v_rcp_f32_e32 v92, v93
	v_add_f32_e32 v93, 1.0, v95
	v_rcp_f32_e32 v95, v93
	v_add_f32_e32 v93, 1.0, v96
	v_mul_f32_e32 v96, 0xbfb8aa3b, v86
	v_exp_f32_e32 v96, v96
	v_exp_f32_e32 v97, v97
	v_mul_f32_e32 v99, 0xbfb8aa3b, v83
	v_exp_f32_e32 v100, v99
	v_add_f32_e32 v96, 1.0, v96
	v_rcp_f32_e32 v98, v96
	v_add_f32_e32 v96, 1.0, v97
	v_mul_f32_e32 v97, 0xbfb8aa3b, v87
	v_exp_f32_e32 v97, v97
	v_rcp_f32_e32 v93, v93
	v_rcp_f32_e32 v96, v96
	v_add_f32_e32 v97, 1.0, v97
	v_rcp_f32_e32 v99, v97
	v_add_f32_e32 v97, 1.0, v100
	v_rcp_f32_e32 v97, v97

.LBB0_401:
	s_nop 0
	v_cvt_pk_bf16_f32 v80, v94, v95
	v_cvt_pk_bf16_f32 v81, v98, v99
	v_cvt_pk_bf16_f32 v82, v92, v93
	v_cvt_pk_bf16_f32 v83, v96, v97
	global_store_dwordx4 v[90:91], v[80:83], off offset:256 sc1
	v_pk_add_f32 v[76:77], v[76:77], v[44:45]
	s_and_b64 vcc, exec, s[8:9]
	v_pk_add_f32 v[80:81], v[78:79], v[46:47]
	v_pk_add_f32 v[78:79], v[74:75], v[42:43]
	v_pk_add_f32 v[74:75], v[72:73], v[40:41]
	s_mov_b64 s[30:31], -1
	s_cbranch_vccnz .LBB0_405
	s_and_b64 vcc, exec, s[4:5]
	v_mov_b32_e32 v89, v79
	v_mov_b32_e32 v88, v78
	v_mov_b32_e32 v86, v75
	v_mov_b32_e32 v84, v74
	v_mov_b32_e32 v91, v81
	v_mov_b32_e32 v90, v80
	v_mov_b32_e32 v87, v77
	v_mov_b32_e32 v85, v76
	s_cbranch_vccnz .LBB0_404
	v_mul_f32_e32 v72, 0xbfb8aa3b, v76
	v_exp_f32_e32 v72, v72
	v_mul_f32_e32 v73, 0xbfb8aa3b, v74
	v_exp_f32_e32 v73, v73
	v_mul_f32_e32 v82, 0xbfb8aa3b, v75
	v_add_f32_e32 v72, 1.0, v72
	v_rcp_f32_e32 v85, v72
	v_mul_f32_e32 v72, 0xbfb8aa3b, v77
	v_exp_f32_e32 v72, v72
	v_exp_f32_e32 v82, v82
	v_add_f32_e32 v73, 1.0, v73
	v_rcp_f32_e32 v84, v73
	v_add_f32_e32 v72, 1.0, v72
	v_mul_f32_e32 v73, 0xbfb8aa3b, v80
	v_rcp_f32_e32 v87, v72
	v_add_f32_e32 v72, 1.0, v82
	v_exp_f32_e32 v73, v73
	v_mul_f32_e32 v82, 0xbfb8aa3b, v78
	v_exp_f32_e32 v82, v82
	v_rcp_f32_e32 v86, v72
	v_add_f32_e32 v72, 1.0, v73
	v_mul_f32_e32 v73, 0xbfb8aa3b, v81
	v_rcp_f32_e32 v90, v72
	v_add_f32_e32 v72, 1.0, v82
	v_exp_f32_e32 v73, v73
	v_mul_f32_e32 v82, 0xbfb8aa3b, v79
	v_exp_f32_e32 v82, v82
	v_rcp_f32_e32 v88, v72
	v_add_f32_e32 v72, 1.0, v73
	v_rcp_f32_e32 v91, v72
	v_add_f32_e32 v72, 1.0, v82
	v_rcp_f32_e32 v89, v72

.LBB0_411:
	v_mov_b64_e32 v[74:75], s[20:21]
	v_mad_i64_i32 v[74:75], s[30:31], v82, s51, v[74:75]
	v_lshl_add_u64 v[74:75], v[146:147], 1, v[74:75]
	v_cvt_pk_bf16_f32 v76, v85, v87
	v_cvt_pk_bf16_f32 v77, v90, v91
	v_cvt_pk_bf16_f32 v78, v84, v86
	v_cvt_pk_bf16_f32 v79, v88, v89
	v_pk_add_f32 v[70:71], v[70:71], v[30:31]
	v_pk_add_f32 v[68:69], v[68:69], v[28:29]
	v_pk_add_f32 v[66:67], v[66:67], v[26:27]
	v_pk_add_f32 v[64:65], v[64:65], v[24:25]
	s_and_b64 vcc, exec, s[6:7]
	s_mov_b64 s[30:31], -1
	global_store_dwordx4 v[74:75], v[76:79], off sc1
	s_cbranch_vccnz .LBB0_415
	s_and_b64 vcc, exec, s[4:5]
	v_mov_b32_e32 v81, v67
	v_mov_b32_e32 v80, v66
	v_mov_b32_e32 v77, v65
	v_mov_b32_e32 v76, v64
	v_mov_b32_e32 v83, v71
	v_mov_b32_e32 v82, v70
	v_mov_b32_e32 v79, v69
	v_mov_b32_e32 v78, v68
	s_cbranch_vccnz .LBB0_414
	v_mul_f32_e32 v76, 0xbfb8aa3b, v68
	v_exp_f32_e32 v76, v76
	v_mul_f32_e32 v77, 0xbfb8aa3b, v64
	v_exp_f32_e32 v77, v77
	v_mul_f32_e32 v81, 0xbfb8aa3b, v66
	v_add_f32_e32 v76, 1.0, v76
	v_rcp_f32_e32 v78, v76
	v_mul_f32_e32 v76, 0xbfb8aa3b, v69
	v_exp_f32_e32 v79, v76
	v_mul_f32_e32 v76, 0xbfb8aa3b, v65
	v_exp_f32_e32 v80, v76
	v_add_f32_e32 v77, 1.0, v77
	v_rcp_f32_e32 v76, v77
	v_add_f32_e32 v77, 1.0, v79
	v_rcp_f32_e32 v79, v77
	v_add_f32_e32 v77, 1.0, v80
	v_mul_f32_e32 v80, 0xbfb8aa3b, v70
	v_exp_f32_e32 v80, v80
	v_exp_f32_e32 v81, v81
	v_mul_f32_e32 v83, 0xbfb8aa3b, v67
	v_exp_f32_e32 v84, v83
	v_add_f32_e32 v80, 1.0, v80
	v_rcp_f32_e32 v82, v80
	v_add_f32_e32 v80, 1.0, v81
	v_mul_f32_e32 v81, 0xbfb8aa3b, v71
	v_exp_f32_e32 v81, v81
	v_rcp_f32_e32 v77, v77
	v_rcp_f32_e32 v80, v80
	v_add_f32_e32 v81, 1.0, v81
	v_rcp_f32_e32 v83, v81
	v_add_f32_e32 v81, 1.0, v84
	v_rcp_f32_e32 v81, v81

.LBB0_419:
	s_nop 0
	v_cvt_pk_bf16_f32 v64, v78, v79
	v_cvt_pk_bf16_f32 v65, v82, v83
	v_cvt_pk_bf16_f32 v66, v76, v77
	v_cvt_pk_bf16_f32 v67, v80, v81
	global_store_dwordx4 v[74:75], v[64:67], off offset:256 sc1
	v_pk_add_f32 v[60:61], v[60:61], v[44:45]
	s_and_b64 vcc, exec, s[8:9]
	v_pk_add_f32 v[64:65], v[62:63], v[46:47]
	v_pk_add_f32 v[62:63], v[58:59], v[42:43]
	v_pk_add_f32 v[58:59], v[56:57], v[40:41]
	s_mov_b64 s[30:31], -1
	s_cbranch_vccnz .LBB0_423
	s_and_b64 vcc, exec, s[4:5]
	v_mov_b32_e32 v73, v63
	v_mov_b32_e32 v72, v62
	v_mov_b32_e32 v70, v59
	v_mov_b32_e32 v68, v58
	v_mov_b32_e32 v75, v65
	v_mov_b32_e32 v74, v64
	v_mov_b32_e32 v71, v61
	v_mov_b32_e32 v69, v60
	s_cbranch_vccnz .LBB0_422
	v_mul_f32_e32 v56, 0xbfb8aa3b, v60
	v_exp_f32_e32 v56, v56
	v_mul_f32_e32 v57, 0xbfb8aa3b, v58
	v_exp_f32_e32 v57, v57
	v_mul_f32_e32 v66, 0xbfb8aa3b, v59
	v_add_f32_e32 v56, 1.0, v56
	v_rcp_f32_e32 v69, v56
	v_mul_f32_e32 v56, 0xbfb8aa3b, v61
	v_exp_f32_e32 v56, v56
	v_exp_f32_e32 v66, v66
	v_add_f32_e32 v57, 1.0, v57
	v_rcp_f32_e32 v68, v57
	v_add_f32_e32 v56, 1.0, v56
	v_mul_f32_e32 v57, 0xbfb8aa3b, v64
	v_rcp_f32_e32 v71, v56
	v_add_f32_e32 v56, 1.0, v66
	v_exp_f32_e32 v57, v57
	v_mul_f32_e32 v66, 0xbfb8aa3b, v62
	v_exp_f32_e32 v66, v66
	v_rcp_f32_e32 v70, v56
	v_add_f32_e32 v56, 1.0, v57
	v_mul_f32_e32 v57, 0xbfb8aa3b, v65
	v_rcp_f32_e32 v74, v56
	v_add_f32_e32 v56, 1.0, v66
	v_exp_f32_e32 v57, v57
	v_mul_f32_e32 v66, 0xbfb8aa3b, v63
	v_exp_f32_e32 v66, v66
	v_rcp_f32_e32 v72, v56
	v_add_f32_e32 v56, 1.0, v57
	v_rcp_f32_e32 v75, v56
	v_add_f32_e32 v56, 1.0, v66
	v_rcp_f32_e32 v73, v56

.LBB0_429:
	v_mov_b64_e32 v[58:59], s[20:21]
	v_mad_i64_i32 v[58:59], s[30:31], v66, s51, v[58:59]
	v_lshl_add_u64 v[58:59], v[146:147], 1, v[58:59]
	v_cvt_pk_bf16_f32 v60, v69, v71
	v_cvt_pk_bf16_f32 v61, v74, v75
	v_cvt_pk_bf16_f32 v62, v68, v70
	v_cvt_pk_bf16_f32 v63, v72, v73
	v_pk_add_f32 v[54:55], v[54:55], v[30:31]
	v_pk_add_f32 v[52:53], v[52:53], v[28:29]
	v_pk_add_f32 v[50:51], v[50:51], v[26:27]
	v_pk_add_f32 v[48:49], v[48:49], v[24:25]
	s_and_b64 vcc, exec, s[6:7]
	s_mov_b64 s[30:31], -1
	global_store_dwordx4 v[58:59], v[60:63], off sc1
	s_cbranch_vccnz .LBB0_433
	s_and_b64 vcc, exec, s[4:5]
	v_mov_b32_e32 v65, v51
	v_mov_b32_e32 v64, v50
	v_mov_b32_e32 v61, v49
	v_mov_b32_e32 v60, v48
	v_mov_b32_e32 v67, v55
	v_mov_b32_e32 v66, v54
	v_mov_b32_e32 v63, v53
	v_mov_b32_e32 v62, v52
	s_cbranch_vccnz .LBB0_432
	v_mul_f32_e32 v60, 0xbfb8aa3b, v52
	v_exp_f32_e32 v60, v60
	v_mul_f32_e32 v61, 0xbfb8aa3b, v48
	v_exp_f32_e32 v61, v61
	v_mul_f32_e32 v65, 0xbfb8aa3b, v50
	v_add_f32_e32 v60, 1.0, v60
	v_rcp_f32_e32 v62, v60
	v_mul_f32_e32 v60, 0xbfb8aa3b, v53
	v_exp_f32_e32 v63, v60
	v_mul_f32_e32 v60, 0xbfb8aa3b, v49
	v_exp_f32_e32 v64, v60
	v_add_f32_e32 v61, 1.0, v61
	v_rcp_f32_e32 v60, v61
	v_add_f32_e32 v61, 1.0, v63
	v_rcp_f32_e32 v63, v61
	v_add_f32_e32 v61, 1.0, v64
	v_mul_f32_e32 v64, 0xbfb8aa3b, v54
	v_exp_f32_e32 v64, v64
	v_exp_f32_e32 v65, v65
	v_mul_f32_e32 v67, 0xbfb8aa3b, v51
	v_exp_f32_e32 v68, v67
	v_add_f32_e32 v64, 1.0, v64
	v_rcp_f32_e32 v66, v64
	v_add_f32_e32 v64, 1.0, v65
	v_mul_f32_e32 v65, 0xbfb8aa3b, v55
	v_exp_f32_e32 v65, v65
	v_rcp_f32_e32 v61, v61
	v_rcp_f32_e32 v64, v64
	v_add_f32_e32 v65, 1.0, v65
	v_rcp_f32_e32 v67, v65
	v_add_f32_e32 v65, 1.0, v68
	v_rcp_f32_e32 v65, v65

.LBB0_437:
	s_nop 0
	v_cvt_pk_bf16_f32 v48, v62, v63
	v_cvt_pk_bf16_f32 v49, v66, v67
	v_cvt_pk_bf16_f32 v50, v60, v61
	v_cvt_pk_bf16_f32 v51, v64, v65
	global_store_dwordx4 v[58:59], v[48:51], off offset:256 sc1
	v_pk_add_f32 v[36:37], v[36:37], v[44:45]
	s_and_b64 vcc, exec, s[8:9]
	v_pk_add_f32 v[48:49], v[38:39], v[46:47]
	v_pk_add_f32 v[38:39], v[34:35], v[42:43]
	v_pk_add_f32 v[34:35], v[32:33], v[40:41]
	s_mov_b64 s[30:31], -1
	s_cbranch_vccnz .LBB0_441
	s_and_b64 vcc, exec, s[4:5]
	v_mov_b32_e32 v57, v39
	v_mov_b32_e32 v56, v38
	v_mov_b32_e32 v54, v35
	v_mov_b32_e32 v52, v34
	v_mov_b32_e32 v59, v49
	v_mov_b32_e32 v58, v48
	v_mov_b32_e32 v55, v37
	v_mov_b32_e32 v53, v36
	s_cbranch_vccnz .LBB0_440
	v_mul_f32_e32 v32, 0xbfb8aa3b, v36
	v_exp_f32_e32 v32, v32
	v_mul_f32_e32 v33, 0xbfb8aa3b, v34
	v_exp_f32_e32 v33, v33
	v_mul_f32_e32 v50, 0xbfb8aa3b, v35
	v_add_f32_e32 v32, 1.0, v32
	v_rcp_f32_e32 v53, v32
	v_mul_f32_e32 v32, 0xbfb8aa3b, v37
	v_exp_f32_e32 v32, v32
	v_exp_f32_e32 v50, v50
	v_add_f32_e32 v33, 1.0, v33
	v_rcp_f32_e32 v52, v33
	v_add_f32_e32 v32, 1.0, v32
	v_mul_f32_e32 v33, 0xbfb8aa3b, v48
	v_rcp_f32_e32 v55, v32
	v_add_f32_e32 v32, 1.0, v50
	v_exp_f32_e32 v33, v33
	v_mul_f32_e32 v50, 0xbfb8aa3b, v38
	v_exp_f32_e32 v50, v50
	v_rcp_f32_e32 v54, v32
	v_add_f32_e32 v32, 1.0, v33
	v_mul_f32_e32 v33, 0xbfb8aa3b, v49
	v_rcp_f32_e32 v58, v32
	v_add_f32_e32 v32, 1.0, v50
	v_exp_f32_e32 v33, v33
	v_mul_f32_e32 v50, 0xbfb8aa3b, v39
	v_exp_f32_e32 v50, v50
	v_rcp_f32_e32 v56, v32
	v_add_f32_e32 v32, 1.0, v33
	v_rcp_f32_e32 v59, v32
	v_add_f32_e32 v32, 1.0, v50
	v_rcp_f32_e32 v57, v32

.LBB0_447:
	v_mov_b64_e32 v[34:35], s[20:21]
	v_mad_i64_i32 v[34:35], s[30:31], v50, s51, v[34:35]
	v_lshl_add_u64 v[34:35], v[146:147], 1, v[34:35]
	v_cvt_pk_bf16_f32 v36, v53, v55
	v_cvt_pk_bf16_f32 v37, v58, v59
	v_cvt_pk_bf16_f32 v38, v52, v54
	v_cvt_pk_bf16_f32 v39, v56, v57
	v_pk_add_f32 v[22:23], v[22:23], v[30:31]
	v_pk_add_f32 v[20:21], v[20:21], v[28:29]
	v_pk_add_f32 v[18:19], v[18:19], v[26:27]
	v_pk_add_f32 v[16:17], v[16:17], v[24:25]
	s_and_b64 vcc, exec, s[6:7]
	s_mov_b64 s[30:31], -1
	global_store_dwordx4 v[34:35], v[36:39], off sc1
	s_cbranch_vccnz .LBB0_451
	s_and_b64 vcc, exec, s[4:5]
	v_mov_b32_e32 v49, v19
	v_mov_b32_e32 v48, v18
	v_mov_b32_e32 v37, v17
	v_mov_b32_e32 v36, v16
	v_mov_b32_e32 v51, v23
	v_mov_b32_e32 v50, v22
	v_mov_b32_e32 v39, v21
	v_mov_b32_e32 v38, v20
	s_cbranch_vccnz .LBB0_450
	v_mul_f32_e32 v36, 0xbfb8aa3b, v20
	v_exp_f32_e32 v36, v36
	v_mul_f32_e32 v37, 0xbfb8aa3b, v16
	v_exp_f32_e32 v37, v37
	v_mul_f32_e32 v49, 0xbfb8aa3b, v18
	v_add_f32_e32 v36, 1.0, v36
	v_rcp_f32_e32 v38, v36
	v_mul_f32_e32 v36, 0xbfb8aa3b, v21
	v_exp_f32_e32 v39, v36
	v_mul_f32_e32 v36, 0xbfb8aa3b, v17
	v_exp_f32_e32 v48, v36
	v_add_f32_e32 v37, 1.0, v37
	v_rcp_f32_e32 v36, v37
	v_add_f32_e32 v37, 1.0, v39
	v_rcp_f32_e32 v39, v37
	v_add_f32_e32 v37, 1.0, v48
	v_mul_f32_e32 v48, 0xbfb8aa3b, v22
	v_exp_f32_e32 v48, v48
	v_exp_f32_e32 v49, v49
	v_mul_f32_e32 v51, 0xbfb8aa3b, v19
	v_exp_f32_e32 v52, v51
	v_add_f32_e32 v48, 1.0, v48
	v_rcp_f32_e32 v50, v48
	v_add_f32_e32 v48, 1.0, v49
	v_mul_f32_e32 v49, 0xbfb8aa3b, v23
	v_exp_f32_e32 v49, v49
	v_rcp_f32_e32 v37, v37
	v_rcp_f32_e32 v48, v48
	v_add_f32_e32 v49, 1.0, v49
	v_rcp_f32_e32 v51, v49
	v_add_f32_e32 v49, 1.0, v52
	v_rcp_f32_e32 v49, v49

.LBB0_455:
	s_nop 0
	v_cvt_pk_bf16_f32 v16, v38, v39
	v_cvt_pk_bf16_f32 v17, v50, v51
	v_cvt_pk_bf16_f32 v18, v36, v37
	v_cvt_pk_bf16_f32 v19, v48, v49
	global_store_dwordx4 v[34:35], v[16:19], off offset:256 sc1
	v_pk_add_f32 v[12:13], v[12:13], v[44:45]
	s_and_b64 vcc, exec, s[8:9]
	v_pk_add_f32 v[16:17], v[14:15], v[46:47]
	v_pk_add_f32 v[14:15], v[10:11], v[42:43]
	v_pk_add_f32 v[10:11], v[8:9], v[40:41]
	s_mov_b64 s[8:9], -1
	s_cbranch_vccnz .LBB0_459
	s_and_b64 vcc, exec, s[4:5]
	v_mov_b32_e32 v33, v15
	v_mov_b32_e32 v32, v14
	v_mov_b32_e32 v22, v11
	v_mov_b32_e32 v20, v10
	v_mov_b32_e32 v35, v17
	v_mov_b32_e32 v34, v16
	v_mov_b32_e32 v23, v13
	v_mov_b32_e32 v21, v12
	s_cbranch_vccnz .LBB0_458
	v_mul_f32_e32 v8, 0xbfb8aa3b, v12
	v_exp_f32_e32 v8, v8
	v_mul_f32_e32 v9, 0xbfb8aa3b, v10
	v_exp_f32_e32 v9, v9
	v_mul_f32_e32 v18, 0xbfb8aa3b, v11
	v_add_f32_e32 v8, 1.0, v8
	v_rcp_f32_e32 v21, v8
	v_mul_f32_e32 v8, 0xbfb8aa3b, v13
	v_exp_f32_e32 v8, v8
	v_exp_f32_e32 v18, v18
	v_add_f32_e32 v9, 1.0, v9
	v_rcp_f32_e32 v20, v9
	v_add_f32_e32 v8, 1.0, v8
	v_mul_f32_e32 v9, 0xbfb8aa3b, v16
	v_rcp_f32_e32 v23, v8
	v_add_f32_e32 v8, 1.0, v18
	v_exp_f32_e32 v9, v9
	v_mul_f32_e32 v18, 0xbfb8aa3b, v14
	v_exp_f32_e32 v18, v18
	v_rcp_f32_e32 v22, v8
	v_add_f32_e32 v8, 1.0, v9
	v_mul_f32_e32 v9, 0xbfb8aa3b, v17
	v_rcp_f32_e32 v34, v8
	v_add_f32_e32 v8, 1.0, v18
	v_exp_f32_e32 v9, v9
	v_mul_f32_e32 v18, 0xbfb8aa3b, v15
	v_exp_f32_e32 v18, v18
	v_rcp_f32_e32 v32, v8
	v_add_f32_e32 v8, 1.0, v9
	v_rcp_f32_e32 v35, v8
	v_add_f32_e32 v8, 1.0, v18
	v_rcp_f32_e32 v33, v8

.LBB0_465:
	v_mov_b64_e32 v[10:11], s[20:21]
	v_mad_i64_i32 v[10:11], s[8:9], v18, s51, v[10:11]
	v_lshl_add_u64 v[10:11], v[146:147], 1, v[10:11]
	v_cvt_pk_bf16_f32 v12, v21, v23
	v_cvt_pk_bf16_f32 v13, v34, v35
	v_cvt_pk_bf16_f32 v14, v20, v22
	v_cvt_pk_bf16_f32 v15, v32, v33
	v_pk_add_f32 v[6:7], v[6:7], v[30:31]
	v_pk_add_f32 v[4:5], v[4:5], v[28:29]
	v_pk_add_f32 v[2:3], v[2:3], v[26:27]
	v_pk_add_f32 v[0:1], v[0:1], v[24:25]
	s_and_b64 vcc, exec, s[6:7]
	s_mov_b64 s[6:7], -1
	global_store_dwordx4 v[10:11], v[12:15], off sc1
	s_cbranch_vccnz .LBB0_469
	s_and_b64 vcc, exec, s[4:5]
	v_mov_b32_e32 v17, v3
	v_mov_b32_e32 v16, v2
	v_mov_b32_e32 v13, v1
	v_mov_b32_e32 v12, v0
	v_mov_b32_e32 v19, v7
	v_mov_b32_e32 v18, v6
	v_mov_b32_e32 v15, v5
	v_mov_b32_e32 v14, v4
	s_cbranch_vccnz .LBB0_468
	v_mul_f32_e32 v12, 0xbfb8aa3b, v4
	v_exp_f32_e32 v12, v12
	v_mul_f32_e32 v13, 0xbfb8aa3b, v0
	v_exp_f32_e32 v13, v13
	v_mul_f32_e32 v17, 0xbfb8aa3b, v2
	v_add_f32_e32 v12, 1.0, v12
	v_rcp_f32_e32 v14, v12
	v_mul_f32_e32 v12, 0xbfb8aa3b, v5
	v_exp_f32_e32 v15, v12
	v_mul_f32_e32 v12, 0xbfb8aa3b, v1
	v_exp_f32_e32 v16, v12
	v_add_f32_e32 v13, 1.0, v13
	v_rcp_f32_e32 v12, v13
	v_add_f32_e32 v13, 1.0, v15
	v_rcp_f32_e32 v15, v13
	v_add_f32_e32 v13, 1.0, v16
	v_mul_f32_e32 v16, 0xbfb8aa3b, v6
	v_exp_f32_e32 v16, v16
	v_exp_f32_e32 v17, v17
	v_mul_f32_e32 v19, 0xbfb8aa3b, v3
	v_exp_f32_e32 v20, v19
	v_add_f32_e32 v16, 1.0, v16
	v_rcp_f32_e32 v18, v16
	v_add_f32_e32 v16, 1.0, v17
	v_mul_f32_e32 v17, 0xbfb8aa3b, v7
	v_exp_f32_e32 v17, v17
	v_rcp_f32_e32 v13, v13
	v_rcp_f32_e32 v16, v16
	v_add_f32_e32 v17, 1.0, v17
	v_rcp_f32_e32 v19, v17
	v_add_f32_e32 v17, 1.0, v20
	v_rcp_f32_e32 v17, v17

.LBB0_473:
	s_nop 0
	v_cvt_pk_bf16_f32 v0, v14, v15
	v_cvt_pk_bf16_f32 v1, v18, v19
	v_cvt_pk_bf16_f32 v2, v12, v13
	v_cvt_pk_bf16_f32 v3, v16, v17
	s_and_b64 vcc, exec, s[2:3]
	s_mov_b64 s[2:3], -1
	global_store_dwordx4 v[10:11], v[0:3], off offset:256 sc1
	s_cbranch_vccnz .LBB0_320
	s_andn2_b64 vcc, exec, s[10:11]
	v_mov_b64 v[136:137], 0
	v_mov_b64 v[138:139], 0
	v_mov_b64 v[140:141], 0
	v_mov_b64 v[142:143], 0
	v_mov_b64 v[124:125], 0
	v_mov_b64 v[126:127], 0
	v_mov_b64 v[120:121], 0
	v_mov_b64 v[122:123], 0
	v_mov_b64 v[108:109], 0
	v_mov_b64 v[110:111], 0
	v_mov_b64 v[104:105], 0
	v_mov_b64 v[106:107], 0
	v_mov_b64 v[92:93], 0
	v_mov_b64 v[94:95], 0
	v_mov_b64 v[88:89], 0
	v_mov_b64 v[90:91], 0
	v_mov_b64 v[132:133], 0
	v_mov_b64 v[134:135], 0
	v_mov_b64 v[128:129], 0
	v_mov_b64 v[130:131], 0
	v_mov_b64 v[116:117], 0
	v_mov_b64 v[118:119], 0
	v_mov_b64 v[112:113], 0
	v_mov_b64 v[114:115], 0
	v_mov_b64 v[100:101], 0
	v_mov_b64 v[102:103], 0
	v_mov_b64 v[96:97], 0
	v_mov_b64 v[98:99], 0
	v_mov_b64 v[84:85], 0
	v_mov_b64 v[86:87], 0
	v_mov_b64 v[80:81], 0
	v_mov_b64 v[82:83], 0
	v_mov_b64 v[76:77], 0
	v_mov_b64 v[78:79], 0
	v_mov_b64 v[72:73], 0
	v_mov_b64 v[74:75], 0
	v_mov_b64 v[60:61], 0
	v_mov_b64 v[62:63], 0
	v_mov_b64 v[56:57], 0
	v_mov_b64 v[58:59], 0
	v_mov_b64 v[36:37], 0
	v_mov_b64 v[38:39], 0
	v_mov_b64 v[32:33], 0
	v_mov_b64 v[34:35], 0
	v_mov_b64 v[12:13], 0
	v_mov_b64 v[14:15], 0
	v_mov_b64 v[8:9], 0
	v_mov_b64 v[10:11], 0
	v_mov_b64 v[68:69], 0
	v_mov_b64 v[70:71], 0
	v_mov_b64 v[64:65], 0
	v_mov_b64 v[66:67], 0
	v_mov_b64 v[52:53], 0
	v_mov_b64 v[54:55], 0
	v_mov_b64 v[48:49], 0
	v_mov_b64 v[50:51], 0
	v_mov_b64 v[20:21], 0
	v_mov_b64 v[22:23], 0
	v_mov_b64 v[16:17], 0
	v_mov_b64 v[18:19], 0
	v_mov_b64 v[4:5], 0
	v_mov_b64 v[6:7], 0
	v_mov_b64 v[0:1], 0
	v_mov_b64 v[2:3], 0
	s_cbranch_vccnz .LBB0_319
	s_barrier
	s_branch .LBB0_319
